# attention: DMA issue block behind the K ds_reads + row-max swap moved into the rare rebase path (later code kept at the same 128-byte phase)
# speedup vs baseline: 1.0032x; 1.0032x over previous
; __device__ __forceinline__ void attn_unit(const Frame& F, const bf16* __restrict__ proj, bf16* mix, const float* relb, const float* subg, int h, int qb, float lam, float one_m_li) {
;     ...
;             if (j == 0 || __any(mx > 8.0f)) {
;                 const float dl = (j == 0) ? mx : fmaxf(mx, 0.f); mrun += dl;
;                 const float alpha = __builtin_amdgcn_exp2f(-dl); lsum *= alpha;
; #pragma unroll
;                 for (int r = 0; r < 16; ++r) { p0[r] -= dl; p1[r] -= dl; negm[r] = -mrun; }
; #pragma unroll
;                 for (int eb = 0; eb < 4; ++eb)
; #pragma unroll
;                     for (int r = 0; r < 16; ++r) o[eb][r] *= alpha;
;             }
.LBB0_590:
	s_nop 7
	v_max_f32_e32 v168, v97, v97
	v_max_f32_e32 v169, v96, v96
	v_max_f32_e32 v168, v169, v168
	v_max3_f32 v169, v98, v99, v81
	v_max3_f32 v168, v168, v80, v82
	v_max3_f32 v168, v168, v83, v100
	v_max3_f32 v169, v169, v102, v103
	v_max3_f32 v168, v168, v101, v84
	v_max3_f32 v169, v169, v86, v87
	v_max3_f32 v168, v168, v85, v104
	v_max3_f32 v169, v169, v106, v107
	v_max3_f32 v168, v168, v105, v88
	v_max3_f32 v169, v169, v90, v91
	v_max3_f32 v168, v168, v89, v108
	v_max3_f32 v169, v169, v110, v111
	v_max3_f32 v168, v168, v109, v92
	v_max3_f32 v169, v169, v94, v95
	v_max3_f32 v168, v168, v93, v169
	s_mov_b32 s8, 0x41000000
	v_cmp_lt_f32_e32 vcc, s8, v168
	s_cbranch_vccz .LBB0_579
	v_mov_b32_e32 v169, v168
	s_nop 1
	v_permlane32_swap_b32 v168, v169
	v_max_f32_e32 v169, v169, v169
	v_max_f32_e32 v168, v168, v168
	v_max_f32_e32 v168, v168, v169
	v_max_f32_e32 v64, v168, v168
	v_max_f32_e32 v66, 0, v64
	v_exp_f32_e64 v68, -v66
	v_add_f32_e32 v162, v162, v66
	v_xor_b32_e32 v64, 0x80000000, v162
	v_pk_add_f32 v[96:97], v[96:97], v[66:67] op_sel_hi:[1,0] neg_lo:[0,1] neg_hi:[0,1]
	v_pk_add_f32 v[80:81], v[80:81], v[66:67] op_sel_hi:[1,0] neg_lo:[0,1] neg_hi:[0,1]
	v_pk_add_f32 v[98:99], v[98:99], v[66:67] op_sel_hi:[1,0] neg_lo:[0,1] neg_hi:[0,1]
	v_pk_add_f32 v[82:83], v[82:83], v[66:67] op_sel_hi:[1,0] neg_lo:[0,1] neg_hi:[0,1]
	v_pk_add_f32 v[100:101], v[100:101], v[66:67] op_sel_hi:[1,0] neg_lo:[0,1] neg_hi:[0,1]
	v_pk_add_f32 v[84:85], v[84:85], v[66:67] op_sel_hi:[1,0] neg_lo:[0,1] neg_hi:[0,1]
	v_pk_add_f32 v[102:103], v[102:103], v[66:67] op_sel_hi:[1,0] neg_lo:[0,1] neg_hi:[0,1]
	v_pk_add_f32 v[86:87], v[86:87], v[66:67] op_sel_hi:[1,0] neg_lo:[0,1] neg_hi:[0,1]
	v_pk_add_f32 v[104:105], v[104:105], v[66:67] op_sel_hi:[1,0] neg_lo:[0,1] neg_hi:[0,1]
	v_pk_add_f32 v[88:89], v[88:89], v[66:67] op_sel_hi:[1,0] neg_lo:[0,1] neg_hi:[0,1]
	v_pk_add_f32 v[106:107], v[106:107], v[66:67] op_sel_hi:[1,0] neg_lo:[0,1] neg_hi:[0,1]
	v_pk_add_f32 v[90:91], v[90:91], v[66:67] op_sel_hi:[1,0] neg_lo:[0,1] neg_hi:[0,1]
	v_pk_add_f32 v[108:109], v[108:109], v[66:67] op_sel_hi:[1,0] neg_lo:[0,1] neg_hi:[0,1]
	v_pk_add_f32 v[92:93], v[92:93], v[66:67] op_sel_hi:[1,0] neg_lo:[0,1] neg_hi:[0,1]
	v_pk_add_f32 v[110:111], v[110:111], v[66:67] op_sel_hi:[1,0] neg_lo:[0,1] neg_hi:[0,1]
	v_pk_add_f32 v[94:95], v[94:95], v[66:67] op_sel_hi:[1,0] neg_lo:[0,1] neg_hi:[0,1]
	v_pk_mul_f32 v[62:63], v[62:63], v[68:69] op_sel_hi:[1,0]
	v_pk_mul_f32 v[60:61], v[60:61], v[68:69] op_sel_hi:[1,0]
	v_pk_mul_f32 v[58:59], v[58:59], v[68:69] op_sel_hi:[1,0]
	v_pk_mul_f32 v[56:57], v[56:57], v[68:69] op_sel_hi:[1,0]
	v_pk_mul_f32 v[54:55], v[54:55], v[68:69] op_sel_hi:[1,0]
	v_pk_mul_f32 v[52:53], v[52:53], v[68:69] op_sel_hi:[1,0]
	v_pk_mul_f32 v[50:51], v[50:51], v[68:69] op_sel_hi:[1,0]
	v_pk_mul_f32 v[48:49], v[48:49], v[68:69] op_sel_hi:[1,0]
	v_pk_mul_f32 v[46:47], v[46:47], v[68:69] op_sel_hi:[1,0]
	v_pk_mul_f32 v[44:45], v[44:45], v[68:69] op_sel_hi:[1,0]
	v_pk_mul_f32 v[42:43], v[42:43], v[68:69] op_sel_hi:[1,0]
	v_pk_mul_f32 v[40:41], v[40:41], v[68:69] op_sel_hi:[1,0]
	v_pk_mul_f32 v[38:39], v[38:39], v[68:69] op_sel_hi:[1,0]
	v_pk_mul_f32 v[36:37], v[36:37], v[68:69] op_sel_hi:[1,0]
	v_pk_mul_f32 v[34:35], v[34:35], v[68:69] op_sel_hi:[1,0]
	v_pk_mul_f32 v[32:33], v[32:33], v[68:69] op_sel_hi:[1,0]
	v_pk_mul_f32 v[30:31], v[30:31], v[68:69] op_sel_hi:[1,0]
	v_pk_mul_f32 v[28:29], v[28:29], v[68:69] op_sel_hi:[1,0]
	v_pk_mul_f32 v[26:27], v[26:27], v[68:69] op_sel_hi:[1,0]
	v_pk_mul_f32 v[24:25], v[24:25], v[68:69] op_sel_hi:[1,0]
	v_pk_mul_f32 v[22:23], v[22:23], v[68:69] op_sel_hi:[1,0]
	v_pk_mul_f32 v[20:21], v[20:21], v[68:69] op_sel_hi:[1,0]
	v_pk_mul_f32 v[18:19], v[18:19], v[68:69] op_sel_hi:[1,0]
	v_pk_mul_f32 v[16:17], v[16:17], v[68:69] op_sel_hi:[1,0]
	v_pk_mul_f32 v[14:15], v[14:15], v[68:69] op_sel_hi:[1,0]
	v_pk_mul_f32 v[12:13], v[12:13], v[68:69] op_sel_hi:[1,0]
	v_pk_mul_f32 v[10:11], v[10:11], v[68:69] op_sel_hi:[1,0]
	v_pk_mul_f32 v[8:9], v[8:9], v[68:69] op_sel_hi:[1,0]
	v_pk_mul_f32 v[6:7], v[6:7], v[68:69] op_sel_hi:[1,0]
	v_pk_mul_f32 v[4:5], v[4:5], v[68:69] op_sel_hi:[1,0]
	v_pk_mul_f32 v[2:3], v[2:3], v[68:69] op_sel_hi:[1,0]
	v_pk_mul_f32 v[0:1], v[0:1], v[68:69] op_sel_hi:[1,0]
	v_mul_f32_e32 v163, v163, v68
	v_mov_b32_e32 v65, v64
	v_mov_b32_e32 v66, v64
	v_mov_b32_e32 v67, v64
	v_mov_b32_e32 v68, v64
	v_mov_b32_e32 v69, v64
	v_mov_b32_e32 v70, v64
	v_mov_b32_e32 v71, v64
	v_mov_b32_e32 v72, v64
	v_mov_b32_e32 v73, v64
	v_mov_b32_e32 v74, v64
	v_mov_b32_e32 v75, v64
	v_mov_b32_e32 v76, v64
	v_mov_b32_e32 v77, v64
	v_mov_b32_e32 v78, v64
	v_mov_b32_e32 v79, v64
	s_branch .LBB0_579
	s_nop 0
